# same overlap of streaming sub-phases with attention, but split by workgroup-id bit 3 (half of every XCD in each mode) instead of by XCD parity; plus previous changes
# baseline (speedup 1.0000x reference)
; #define PB_BEGIN(id) unsigned long long _pt0_##id = (((PROBE_MASK) >> (id)) & 1) ? __builtin_amdgcn_s_memrealtime() : 0ull
; #define PB_END(id) do { if (((PROBE_MASK) >> (id)) & 1) { __syncthreads(); const unsigned long long _t1 = __builtin_amdgcn_s_memrealtime(), _w = (_t1 - _pt0_##id) * (PROBE_MUL); \
;         while (__builtin_amdgcn_s_memrealtime() - _t1 < _w) __builtin_amdgcn_s_sleep(8); } } while (0)
; #define PB_BEGIN(id) do {} while (0)
; #define PB_END(id) do {} while (0)
; __global__ void __launch_bounds__(NTHR, 2) fwd_kernel(Params prm) {
;     ...
;             PB_BEGIN(3); launder(F); if (SUB3 & 1) phase_conv(F, P, l, nrows); launder(F); PB_END(3); PB_BEGIN(4);
;             if (SUB3 & 2) phase_fft_a(F);
;             launder(F); if ((SUB3 & 4) && l == 0) phase_ctx_dft(F); launder(F); PB_END(4); PB_BEGIN(5);
;             if (SUB3 & 8) phase_attn(F, P, l);
.LBB0_320:
	s_andn2_b64 vcc, exec, s[8:9]
	s_cbranch_vccnz .LBB0_506
	v_readlane_b32 s100, v254, 62
	s_nop 0
	s_bitcmp1_b32 s100, 3
	s_cbranch_scc0 .Lpb2_conv
	s_movk_i32 s22, 0x400
	s_andn2_b64 vcc, exec, s[64:65]
	s_cbranch_vccnz .Lpb2_attn_entry
	s_movk_i32 s22, 0x420
	s_branch .Lpb2_attn_entry

; #define SEAM(k) do { if (IN((k) + 1)) { xcd_barrier(bar); xcd_barrier(bar); } } while (0)
; #define SEAM(k) do { if (IN((k) + 1)) xcd_barrier(bar); } while (0)
; #define PB_BEGIN(id) unsigned long long _pt0_##id = (((PROBE_MASK) >> (id)) & 1) ? __builtin_amdgcn_s_memrealtime() : 0ull
; #define PB_END(id) do { if (((PROBE_MASK) >> (id)) & 1) { __syncthreads(); const unsigned long long _t1 = __builtin_amdgcn_s_memrealtime(), _w = (_t1 - _pt0_##id) * (PROBE_MUL); \
;         while (__builtin_amdgcn_s_memrealtime() - _t1 < _w) __builtin_amdgcn_s_sleep(8); } } while (0)
; #define PB_BEGIN(id) do {} while (0)
; #define PB_END(id) do {} while (0)
; __global__ void __launch_bounds__(NTHR, 2) fwd_kernel(Params prm) {
;     ...
;             PB_BEGIN(3); launder(F); if (SUB3 & 1) phase_conv(F, P, l, nrows); launder(F); PB_END(3); PB_BEGIN(4);
;             if (SUB3 & 2) phase_fft_a(F);
;             launder(F); if ((SUB3 & 4) && l == 0) phase_ctx_dft(F); launder(F); PB_END(4); PB_BEGIN(5);
;             if (SUB3 & 8) phase_attn(F, P, l);
;             PB_END(5);
;             SEAM(PB + 2);
.LBB0_338:
	v_readlane_b32 s100, v254, 62
	s_nop 0
	s_bitcmp1_b32 s100, 3
	s_cbranch_scc0 .Lpb2_attn_entry
	v_readlane_b32 s7, v245, 0
	v_readlane_b32 s24, v245, 1
	v_readlane_b32 s25, v245, 2
	v_readlane_b32 s28, v245, 3
	v_readlane_b32 s29, v245, 4
	v_readlane_b32 s30, v245, 5
	v_readlane_b32 s31, v245, 6
	v_readlane_b32 s40, v245, 7
	v_readlane_b32 s41, v245, 8
	v_readlane_b32 s42, v245, 9
	v_readlane_b32 s43, v245, 10
	v_readlane_b32 s46, v245, 11
	v_readlane_b32 s47, v245, 12
	v_readlane_b32 s48, v245, 13
	v_readlane_b32 s49, v245, 14
	v_readlane_b32 s50, v245, 15
	v_readlane_b32 s51, v245, 16
	v_readlane_b32 s76, v245, 17
	v_mov_b32_e32 v198, v0
	s_nop 4
	s_branch .Lpb2_seam

; #define SEAM(k) do { if (IN((k) + 1)) { xcd_barrier(bar); xcd_barrier(bar); } } while (0)
; #define SEAM(k) do { if (IN((k) + 1)) xcd_barrier(bar); } while (0)
; #define PB_BEGIN(id) unsigned long long _pt0_##id = (((PROBE_MASK) >> (id)) & 1) ? __builtin_amdgcn_s_memrealtime() : 0ull
; #define PB_END(id) do { if (((PROBE_MASK) >> (id)) & 1) { __syncthreads(); const unsigned long long _t1 = __builtin_amdgcn_s_memrealtime(), _w = (_t1 - _pt0_##id) * (PROBE_MUL); \
;         while (__builtin_amdgcn_s_memrealtime() - _t1 < _w) __builtin_amdgcn_s_sleep(8); } } while (0)
; #define PB_BEGIN(id) do {} while (0)
; #define PB_END(id) do {} while (0)
; __global__ void __launch_bounds__(NTHR, 2) fwd_kernel(Params prm) {
;     ...
;             launder(F); if ((SUB3 & 4) && l == 0) phase_ctx_dft(F); launder(F); PB_END(4); PB_BEGIN(5);
;             if (SUB3 & 8) phase_attn(F, P, l);
;             PB_END(5);
;             SEAM(PB + 2);
.LBB0_456:
	v_readlane_b32 s100, v254, 62
	s_nop 0
	s_bitcmp1_b32 s100, 3
	s_cbranch_scc0 .Lpb2_seam
	v_writelane_b32 v245, s7, 0
	v_writelane_b32 v245, s24, 1
	v_writelane_b32 v245, s25, 2
	v_writelane_b32 v245, s28, 3
	v_writelane_b32 v245, s29, 4
	v_writelane_b32 v245, s30, 5
	v_writelane_b32 v245, s31, 6
	v_writelane_b32 v245, s40, 7
	v_writelane_b32 v245, s41, 8
	v_writelane_b32 v245, s42, 9
	v_writelane_b32 v245, s43, 10
	v_writelane_b32 v245, s46, 11
	v_writelane_b32 v245, s47, 12
	v_writelane_b32 v245, s48, 13
	v_writelane_b32 v245, s49, 14
	v_writelane_b32 v245, s50, 15
	v_writelane_b32 v245, s51, 16
	v_writelane_b32 v245, s76, 17
	s_waitcnt lgkmcnt(0)
	s_barrier
	s_branch .Lpb2_conv
